# speedup vs baseline: 1.0031x; 1.0031x over previous
.LBB2_6:
	s_or_b64 exec, exec, s[18:19]
	v_xor_b32_e32 v23, 32, v23
	s_add_i32 s38, 0, 0x1c000
	v_lshlrev_b32_e32 v23, 2, v23
	v_lshlrev_b32_e32 v199, 2, v25
	s_waitcnt vmcnt(4) lgkmcnt(0)
	s_barrier
	v_add3_u32 v23, s38, v23, v199
	ds_read_b32 v23, v23
	v_max_f32_e32 v24, v24, v24
	v_mul_f32_e32 v22, 0x3db8aa3b, v22
	v_mov_b32_e32 v164, 0
	v_mov_b32_e32 v165, 0
	s_waitcnt lgkmcnt(0)
	s_movk_i32 s45, 0x4000
	v_add3_u32 v250, s45, v184, v185
	v_add3_u32 v251, s45, v184, v186
	v_add3_u32 v252, s45, v184, v187
	v_add3_u32 v253, s45, v184, v188
	ds_read_b128 v[218:221], v250 offset:49152
	ds_read_b128 v[222:225], v251 offset:49152
	ds_read_b128 v[242:245], v252 offset:49152
	ds_read_b128 v[246:249], v253 offset:49152
	v_add3_u32 v250, s45, v184, v189
	v_add3_u32 v251, s45, v184, v190
	v_add3_u32 v252, s45, v184, v191
	v_add3_u32 v253, s45, v184, v192
	ds_read_b128 v[202:205], v250 offset:49152
	ds_read_b128 v[206:209], v251 offset:49152
	ds_read_b128 v[210:213], v252 offset:49152
	ds_read_b128 v[214:217], v253 offset:49152
	v_max_f32_e32 v23, v23, v23
	v_max_f32_e32 v197, v24, v23
	v_mov_b32_e32 v23, 2.0
	v_fmamk_f32 v200, v197, 0xbdb8aa3b, v23
	v_fmamk_f32 v23, v22, 0xcb400000, v200
	v_fma_f32 v2, v2, v22, v23
	v_fma_f32 v3, v3, v22, v23
	v_fma_f32 v6, v6, v22, v23
	v_fma_f32 v7, v7, v22, v23
	v_fma_f32 v10, v10, v22, v23
	v_fma_f32 v11, v11, v22, v23
	v_fma_f32 v14, v14, v22, v23
	v_fma_f32 v15, v15, v22, v23
	v_exp_f32_e32 v2, v2
	v_exp_f32_e32 v3, v3
	v_exp_f32_e32 v6, v6
	v_exp_f32_e32 v7, v7
	v_exp_f32_e32 v10, v10
	v_exp_f32_e32 v11, v11
	v_exp_f32_e32 v14, v14
	v_exp_f32_e32 v15, v15
	v_fma_f32 v4, v4, v22, v23
	v_fma_f32 v5, v5, v22, v23
	v_fma_f32 v8, v8, v22, v23
	v_fma_f32 v9, v9, v22, v23
	v_fma_f32 v12, v12, v22, v23
	v_fma_f32 v13, v13, v22, v23
	v_fma_f32 v16, v16, v22, v23
	v_fmac_f32_e32 v23, v17, v22
	v_mov_b32_e32 v166, 0
	v_mov_b32_e32 v167, 0
	v_exp_f32_e32 v4, v4
	v_exp_f32_e32 v5, v5
	v_exp_f32_e32 v8, v8
	v_exp_f32_e32 v9, v9
	v_exp_f32_e32 v12, v12
	v_exp_f32_e32 v13, v13
	v_exp_f32_e32 v16, v16
	v_exp_f32_e32 v17, v23
	v_add_f32_e32 v250, v2, v3
	v_add_f32_e32 v251, v4, v5
	v_add_f32_e32 v252, v6, v7
	v_add_f32_e32 v253, v8, v9
	v_add_f32_e32 v250, v250, v251
	v_add_f32_e32 v252, v252, v253
	v_add_f32_e32 v251, v10, v11
	v_add_f32_e32 v253, v12, v13
	v_add_f32_e32 v250, v250, v252
	v_add_f32_e32 v251, v251, v253
	v_add_f32_e32 v252, v14, v15
	v_add_f32_e32 v253, v16, v17
	v_add_f32_e32 v250, v250, v251
	v_add_f32_e32 v252, v252, v253
	v_add_f32_e32 v250, v250, v252
	v_cvt_pk_fp8_f32 v164, v2, v3
	v_cvt_pk_fp8_f32 v165, v6, v7
	v_cvt_pk_fp8_f32 v166, v10, v11
	v_cvt_pk_fp8_f32 v167, v14, v15
	s_lshl_b32 s0, s22, 11
	s_add_i32 s0, s0, 0
	s_add_i32 s0, s0, 0x18000
	v_cvt_pk_fp8_f32 v164, v4, v5 op_sel:[0,0,1]
	v_cvt_pk_fp8_f32 v165, v8, v9 op_sel:[0,0,1]
	v_cvt_pk_fp8_f32 v166, v12, v13 op_sel:[0,0,1]
	v_cvt_pk_fp8_f32 v167, v16, v17 op_sel:[0,0,1]
	v_lshl_add_u32 v193, v198, 4, s0
	v_lshrrev_b32_e32 v3, 2, v0
	v_lshlrev_b32_e32 v6, 1, v183
	s_lshl_b32 s0, s20, 20
	v_bfe_u32 v4, v0, 2, 2
	v_lshl_or_b32 v5, v1, 6, s24
	v_bitop3_b32 v3, v6, v3, 3 bitop3:0x78
	s_or_b32 s18, s0, s23
	v_lshl_add_u32 v194, s34, 10, v193
	v_lshl_or_b32 v195, v3, 4, v5
	v_bitop3_b32 v3, v6, v4, 1 bitop3:0x36
	v_add3_u32 v4, s21, v20, v21
	s_add_u32 s0, s6, s18
	ds_write_b128 v194, v[164:167]
	v_lshl_or_b32 v196, v3, 4, v5
	v_ashrrev_i32_e32 v5, 31, v4
	s_addc_u32 s1, s7, 0
	s_waitcnt vmcnt(2) lgkmcnt(0)
	s_barrier
	s_mov_b64 s[60:61], s[0:1]
	v_lshl_add_u64 v[170:171], s[0:1], 0, v[4:5]
	v_add3_u32 v4, s21, v18, v19
	s_add_u32 s0, s8, s18
	v_mov_b32_e32 v2, 0
	v_ashrrev_i32_e32 v5, 31, v4
	s_addc_u32 s1, s9, 0
	s_mov_b32 s39, 0
	s_mov_b32 s40, 1
	s_mov_b64 s[64:65], s[0:1]
	v_lshl_add_u64 v[172:173], s[0:1], 0, v[4:5]
	s_mov_b64 s[6:7], 0
	s_movk_i32 s41, 0x2000
	s_mov_b64 s[8:9], 0xc000
	s_mov_b64 s[18:19], 0xe000
	s_mov_b64 s[20:21], 0x8000
	s_mov_b64 s[22:23], 0xa000
	s_mov_b32 s42, 0x42966666
	v_mov_b32_e32 v82, 0x4b400000
	v_mov_b32_e32 v100, 0x38383838
	s_mov_b32 s0, 0
	s_mov_b32 s43, 1
	v_mov_b32_e32 v3, v2
	v_mov_b32_e32 v4, v2
	v_mov_b32_e32 v5, v2
	v_mov_b32_e32 v6, v2
	v_mov_b32_e32 v7, v2
	v_mov_b32_e32 v8, v2
	v_mov_b32_e32 v9, v2
	v_mov_b32_e32 v10, v2
	v_mov_b32_e32 v11, v2
	v_mov_b32_e32 v12, v2
	v_mov_b32_e32 v13, v2
	v_mov_b32_e32 v14, v2
	v_mov_b32_e32 v15, v2
	v_mov_b32_e32 v16, v2
	v_mov_b32_e32 v17, v2
	v_mov_b32_e32 v18, v2
	v_mov_b32_e32 v19, v2
	v_mov_b32_e32 v20, v2
	v_mov_b32_e32 v21, v2
	v_mov_b32_e32 v22, v2
	v_mov_b32_e32 v23, v2
	v_mov_b32_e32 v24, v2
	v_mov_b32_e32 v25, v2
	v_mov_b32_e32 v26, v2
	v_mov_b32_e32 v27, v2
	v_mov_b32_e32 v28, v2
	v_mov_b32_e32 v29, v2
	v_mov_b32_e32 v30, v2
	v_mov_b32_e32 v31, v2
	v_mov_b32_e32 v32, v2
	v_mov_b32_e32 v33, v2
	v_mov_b32_e32 v34, v2
	v_mov_b32_e32 v35, v2
	v_mov_b32_e32 v36, v2
	v_mov_b32_e32 v37, v2
	v_mov_b32_e32 v38, v2
	v_mov_b32_e32 v39, v2
	v_mov_b32_e32 v40, v2
	v_mov_b32_e32 v41, v2
	v_mov_b32_e32 v42, v2
	v_mov_b32_e32 v43, v2
	v_mov_b32_e32 v44, v2
	v_mov_b32_e32 v45, v2
	v_mov_b32_e32 v46, v2
	v_mov_b32_e32 v47, v2
	v_mov_b32_e32 v48, v2
	v_mov_b32_e32 v49, v2
	v_mov_b32_e32 v50, v2
	v_mov_b32_e32 v51, v2
	v_mov_b32_e32 v52, v2
	v_mov_b32_e32 v53, v2
	v_mov_b32_e32 v54, v2
	v_mov_b32_e32 v55, v2
	v_mov_b32_e32 v56, v2
	v_mov_b32_e32 v57, v2
	v_mov_b32_e32 v58, v2
	v_mov_b32_e32 v59, v2
	v_mov_b32_e32 v60, v2
	v_mov_b32_e32 v61, v2
	v_mov_b32_e32 v62, v2
	v_mov_b32_e32 v63, v2
	v_mov_b32_e32 v64, v2
	v_mov_b32_e32 v65, v2
	v_mov_b32_e32 v66, v2
	v_mov_b32_e32 v67, v2
	v_mov_b32_e32 v68, v2
	v_mov_b32_e32 v69, v2
	v_mov_b32_e32 v70, v2
	v_mov_b32_e32 v71, v2
	v_mov_b32_e32 v72, v2
	v_mov_b32_e32 v73, v2
	v_mov_b32_e32 v74, v2
	v_mov_b32_e32 v75, v2
	v_mov_b32_e32 v76, v2
	v_mov_b32_e32 v77, v2
	v_mov_b32_e32 v78, v2
	v_mov_b32_e32 v79, v2
	v_mov_b32_e32 v80, v2
	v_mov_b32_e32 v81, v2
	v_mov_b32_e32 v66, v250
	v_mov_b32_e32 v226, 0x4b400000
	v_mov_b32_e32 v227, v226
	v_mov_b32_e32 v228, v226
	v_mov_b32_e32 v229, v226
	v_mov_b32_e32 v230, v226
	v_mov_b32_e32 v231, v226
	v_mov_b32_e32 v232, v226
	v_mov_b32_e32 v233, v226
	v_mov_b32_e32 v234, v226
	v_mov_b32_e32 v235, v226
	v_mov_b32_e32 v236, v226
	v_mov_b32_e32 v237, v226
	v_mov_b32_e32 v238, v226
	v_mov_b32_e32 v239, v226
	v_mov_b32_e32 v240, v226
	v_mov_b32_e32 v241, v226
	v_add_u32_e32 v250, 0xc000, v184
	v_add_u32_e32 v185, v185, v250
	v_add_u32_e32 v186, v186, v250
	v_add_u32_e32 v187, v187, v250
	v_add_u32_e32 v188, v188, v250
	v_add_u32_e32 v189, v189, v250
	v_add_u32_e32 v190, v190, v250
	v_add_u32_e32 v191, v191, v250
	v_add_u32_e32 v192, v192, v250
	v_subrev_u32_e32 v252, s60, v170
	v_subrev_u32_e32 v255, s64, v172
	s_sub_u32 s1, s64, s60
	s_add_i32 s1, s1, 0xffffc000
	v_add_u32_e32 v254, 0x2000, v252
	v_add_u32_e32 v255, s1, v255
	v_add_u32_e32 v201, 0x2000, v255
	s_add_u32 s60, s60, 0xc000
	s_addc_u32 s61, s61, 0
	s_mov_b32 s42, 0x43dc0000
	s_mov_b64 s[54:55], -1
	v_mul_f32_e32 v71, 0x3db8aa3b, v168
	v_mov_b32_e32 v72, 0
	v_mfma_i32_32x32x32_i8 v[84:99], v[218:221], v[132:135], v[226:241]
	v_mfma_i32_32x32x32_i8 v[84:99], v[222:225], v[136:139], v[84:99]

.Lat_k0:
	ds_read_b128 v[128:131], v196 offset:4096
	v_mfma_i32_32x32x32_i8 v[84:99], v[202:205], v[148:151], v[84:99]
	ds_read_b128 v[202:205], v195
	v_mfma_i32_32x32x32_i8 v[84:99], v[206:209], v[152:155], v[84:99]
	ds_read_b128 v[206:209], v196
	v_mfma_i32_32x32x32_i8 v[84:99], v[210:213], v[156:159], v[84:99]
	ds_read_b128 v[210:213], v195 offset:2048
	v_mfma_i32_32x32x32_i8 v[84:99], v[214:217], v[160:163], v[84:99]
	ds_read_b128 v[214:217], v196 offset:2048
	v_readlane_b32 s50, v182, s43
	s_waitcnt lgkmcnt(6)
	v_mfma_f32_32x32x64_f8f6f4 v[2:17], v[108:115], v[116:123], v[2:17]
	ds_read_b128 v[218:221], v185 offset:32768
	ds_read_b128 v[222:225], v186 offset:32768
	ds_read_b128 v[242:245], v187 offset:32768
	ds_read_b128 v[246:249], v188 offset:32768
	v_mul_f32_e32 v250, s50, v71
	v_fmamk_f32 v251, v250, 0xcb400000, v200
	s_cmp_gt_u32 s43, 30
	s_cbranch_scc1 .Lat_nov0
	s_add_i32 m0, s31, 32768
	v_fma_f32 v84, v84, v250, v251
	global_load_lds_dwordx4 v255, s[60:61]
	s_add_i32 m0, s31, 40960
	v_fma_f32 v85, v85, v250, v251
	global_load_lds_dwordx4 v201, s[60:61]
	s_branch .Lat_v0

.Lat_v0:
	v_fma_f32 v86, v86, v250, v251
	v_fma_f32 v87, v87, v250, v251
	v_exp_f32_e32 v84, v84
	v_exp_f32_e32 v85, v85
	v_exp_f32_e32 v86, v86
	v_exp_f32_e32 v87, v87
	v_fma_f32 v88, v88, v250, v251
	v_fma_f32 v89, v89, v250, v251
	v_fma_f32 v90, v90, v250, v251
	v_fma_f32 v91, v91, v250, v251
	s_waitcnt lgkmcnt(8)
	v_mfma_f32_32x32x64_f8f6f4 v[18:33], v[108:115], v[124:131], v[18:33]
	v_add_f32_e32 v67, v84, v85
	v_add_f32_e32 v68, v86, v87
	v_exp_f32_e32 v88, v88
	v_exp_f32_e32 v89, v89
	v_exp_f32_e32 v90, v90
	v_exp_f32_e32 v91, v91
	v_add_f32_e32 v67, v67, v68
	v_cvt_pk_fp8_f32 v164, v84, v85
	v_cvt_pk_fp8_f32 v164, v86, v87 op_sel:[0,0,1]
	v_fma_f32 v92, v92, v250, v251
	v_fma_f32 v93, v93, v250, v251
	v_fma_f32 v94, v94, v250, v251
	v_fma_f32 v95, v95, v250, v251
	v_add_f32_e32 v68, v88, v89
	v_add_f32_e32 v69, v90, v91
	s_waitcnt lgkmcnt(6)
	v_mfma_f32_32x32x64_f8f6f4 v[50:65], v[108:115], v[202:209], v[50:65]
	ds_read_b128 v[202:205], v189 offset:32768
	ds_read_b128 v[206:209], v190 offset:32768
	v_exp_f32_e32 v92, v92
	v_exp_f32_e32 v93, v93
	v_exp_f32_e32 v94, v94
	v_exp_f32_e32 v95, v95
	v_add_f32_e32 v68, v68, v69
	v_cvt_pk_fp8_f32 v165, v88, v89
	v_cvt_pk_fp8_f32 v165, v90, v91 op_sel:[0,0,1]
	v_fma_f32 v96, v96, v250, v251
	v_fma_f32 v97, v97, v250, v251
	v_fma_f32 v98, v98, v250, v251
	v_fma_f32 v99, v99, v250, v251
	v_add_f32_e32 v67, v67, v68
	v_add_f32_e32 v68, v92, v93
	v_add_f32_e32 v69, v94, v95
	s_waitcnt lgkmcnt(6)
	v_mfma_f32_32x32x64_f8f6f4 v[34:49], v[108:115], v[210:217], v[34:49]
	ds_read_b128 v[210:213], v191 offset:32768
	ds_read_b128 v[214:217], v192 offset:32768
	v_exp_f32_e32 v96, v96
	v_exp_f32_e32 v97, v97
	v_exp_f32_e32 v98, v98
	v_exp_f32_e32 v99, v99
	v_add_f32_e32 v68, v68, v69
	v_cvt_pk_fp8_f32 v166, v92, v93
	v_cvt_pk_fp8_f32 v166, v94, v95 op_sel:[0,0,1]
	v_add_f32_e32 v67, v67, v68
	v_add_f32_e32 v68, v96, v97
	v_add_f32_e32 v69, v98, v99
	s_add_u32 s60, s60, 0x4000
	s_addc_u32 s61, s61, 0
	v_add_f32_e32 v68, v68, v69
	v_cvt_pk_fp8_f32 v167, v96, v97
	v_cvt_pk_fp8_f32 v167, v98, v99 op_sel:[0,0,1]
	v_add_f32_e32 v67, v67, v68
	ds_write_b128 v194, v[164:167] offset:8192
	v_max_f32_e32 v72, v72, v67
	v_add_f32_e32 v66, v66, v67
	s_add_i32 s43, s43, 1
	s_cmp_eq_u32 s43, 32
	s_cbranch_scc1 .Lat_last
	s_waitcnt lgkmcnt(7)
	v_mfma_i32_32x32x32_i8 v[84:99], v[218:221], v[132:135], v[226:241]
	v_mfma_i32_32x32x32_i8 v[84:99], v[222:225], v[136:139], v[84:99]
	s_waitcnt vmcnt(2) lgkmcnt(0)
	s_barrier
.Lat_u1:
	ds_read_b128 v[108:111], v193 offset:8192
	ds_read_b128 v[112:115], v193 offset:9216
	v_mfma_i32_32x32x32_i8 v[84:99], v[242:245], v[140:143], v[84:99]
	ds_read_b128 v[116:119], v195 offset:22528
	ds_read_b128 v[120:123], v196 offset:22528
	s_add_i32 m0, s31, 65536
	ds_read_b128 v[124:127], v195 offset:20480
	global_load_lds_dwordx4 v252, s[60:61]
	s_add_i32 m0, s31, 73728
	v_mfma_i32_32x32x32_i8 v[84:99], v[246:249], v[144:147], v[84:99]
	global_load_lds_dwordx4 v254, s[60:61]
	ds_read_b128 v[128:131], v196 offset:20480
	v_mfma_i32_32x32x32_i8 v[84:99], v[202:205], v[148:151], v[84:99]
	ds_read_b128 v[202:205], v195 offset:16384
	v_mfma_i32_32x32x32_i8 v[84:99], v[206:209], v[152:155], v[84:99]
	ds_read_b128 v[206:209], v196 offset:16384
	v_mfma_i32_32x32x32_i8 v[84:99], v[210:213], v[156:159], v[84:99]
	ds_read_b128 v[210:213], v195 offset:18432
	v_mfma_i32_32x32x32_i8 v[84:99], v[214:217], v[160:163], v[84:99]
	ds_read_b128 v[214:217], v196 offset:18432
	v_readlane_b32 s50, v182, s43
	s_waitcnt lgkmcnt(6)
	v_mfma_f32_32x32x64_f8f6f4 v[2:17], v[108:115], v[116:123], v[2:17]
	ds_read_b128 v[218:221], v185
	ds_read_b128 v[222:225], v186
	ds_read_b128 v[242:245], v187
	ds_read_b128 v[246:249], v188
	v_mul_f32_e32 v250, s50, v71
	v_fmamk_f32 v251, v250, 0xcb400000, v200
	s_mov_b32 m0, s31
	v_fma_f32 v84, v84, v250, v251
	global_load_lds_dwordx4 v255, s[60:61]
	s_add_i32 m0, s31, 8192
	v_fma_f32 v85, v85, v250, v251
	global_load_lds_dwordx4 v201, s[60:61]
	v_fma_f32 v86, v86, v250, v251
	v_fma_f32 v87, v87, v250, v251
	v_exp_f32_e32 v84, v84
	v_exp_f32_e32 v85, v85
	v_exp_f32_e32 v86, v86
	v_exp_f32_e32 v87, v87
	v_fma_f32 v88, v88, v250, v251
	v_fma_f32 v89, v89, v250, v251
	v_fma_f32 v90, v90, v250, v251
	v_fma_f32 v91, v91, v250, v251
	s_waitcnt lgkmcnt(8)
	v_mfma_f32_32x32x64_f8f6f4 v[18:33], v[108:115], v[124:131], v[18:33]
	v_add_f32_e32 v67, v84, v85
	v_add_f32_e32 v68, v86, v87
	v_exp_f32_e32 v88, v88
	v_exp_f32_e32 v89, v89
	v_exp_f32_e32 v90, v90
	v_exp_f32_e32 v91, v91
	v_add_f32_e32 v67, v67, v68
	v_cvt_pk_fp8_f32 v164, v84, v85
	v_cvt_pk_fp8_f32 v164, v86, v87 op_sel:[0,0,1]
	v_fma_f32 v92, v92, v250, v251
	v_fma_f32 v93, v93, v250, v251
	v_fma_f32 v94, v94, v250, v251
	v_fma_f32 v95, v95, v250, v251
	v_add_f32_e32 v68, v88, v89
	v_add_f32_e32 v69, v90, v91
	s_waitcnt lgkmcnt(6)
	v_mfma_f32_32x32x64_f8f6f4 v[50:65], v[108:115], v[202:209], v[50:65]
	ds_read_b128 v[202:205], v189
	ds_read_b128 v[206:209], v190
	v_exp_f32_e32 v92, v92
	v_exp_f32_e32 v93, v93
	v_exp_f32_e32 v94, v94
	v_exp_f32_e32 v95, v95
	v_add_f32_e32 v68, v68, v69
	v_cvt_pk_fp8_f32 v165, v88, v89
	v_cvt_pk_fp8_f32 v165, v90, v91 op_sel:[0,0,1]
	v_fma_f32 v96, v96, v250, v251
	v_fma_f32 v97, v97, v250, v251
	v_fma_f32 v98, v98, v250, v251
	v_fma_f32 v99, v99, v250, v251
	v_add_f32_e32 v67, v67, v68
	v_add_f32_e32 v68, v92, v93
	v_add_f32_e32 v69, v94, v95
	s_waitcnt lgkmcnt(6)
	v_mfma_f32_32x32x64_f8f6f4 v[34:49], v[108:115], v[210:217], v[34:49]
	ds_read_b128 v[210:213], v191
	ds_read_b128 v[214:217], v192
	v_exp_f32_e32 v96, v96
	v_exp_f32_e32 v97, v97
	v_exp_f32_e32 v98, v98
	v_exp_f32_e32 v99, v99
	v_add_f32_e32 v68, v68, v69
	v_cvt_pk_fp8_f32 v166, v92, v93
	v_cvt_pk_fp8_f32 v166, v94, v95 op_sel:[0,0,1]
	v_add_f32_e32 v67, v67, v68
	v_add_f32_e32 v68, v96, v97
	v_add_f32_e32 v69, v98, v99
	s_add_u32 s60, s60, 0x4000
	s_addc_u32 s61, s61, 0
	v_add_f32_e32 v68, v68, v69
	v_cvt_pk_fp8_f32 v167, v96, v97
	v_cvt_pk_fp8_f32 v167, v98, v99 op_sel:[0,0,1]
	v_add_f32_e32 v67, v67, v68
	ds_write_b128 v194, v[164:167]
	v_max_f32_e32 v72, v72, v67
	v_add_f32_e32 v66, v66, v67
	s_add_i32 s43, s43, 1
	s_waitcnt lgkmcnt(7)
	v_mfma_i32_32x32x32_i8 v[84:99], v[218:221], v[132:135], v[226:241]
	v_mfma_i32_32x32x32_i8 v[84:99], v[222:225], v[136:139], v[84:99]
	s_waitcnt vmcnt(2) lgkmcnt(0)
	s_barrier
.Lat_u2:
	ds_read_b128 v[108:111], v193
	ds_read_b128 v[112:115], v193 offset:1024
	v_mfma_i32_32x32x32_i8 v[84:99], v[242:245], v[140:143], v[84:99]
	ds_read_b128 v[116:119], v195 offset:38912
	ds_read_b128 v[120:123], v196 offset:38912
	s_add_i32 m0, s31, 81920
	ds_read_b128 v[124:127], v195 offset:36864
	global_load_lds_dwordx4 v252, s[60:61]
	s_add_i32 m0, s31, 90112
	v_mfma_i32_32x32x32_i8 v[84:99], v[246:249], v[144:147], v[84:99]
	global_load_lds_dwordx4 v254, s[60:61]
	ds_read_b128 v[128:131], v196 offset:36864
	v_mfma_i32_32x32x32_i8 v[84:99], v[202:205], v[148:151], v[84:99]
	ds_read_b128 v[202:205], v195 offset:32768
	v_mfma_i32_32x32x32_i8 v[84:99], v[206:209], v[152:155], v[84:99]
	ds_read_b128 v[206:209], v196 offset:32768
	v_mfma_i32_32x32x32_i8 v[84:99], v[210:213], v[156:159], v[84:99]
	ds_read_b128 v[210:213], v195 offset:34816
	v_mfma_i32_32x32x32_i8 v[84:99], v[214:217], v[160:163], v[84:99]
	ds_read_b128 v[214:217], v196 offset:34816
	v_readlane_b32 s50, v182, s43
	s_waitcnt lgkmcnt(6)
	v_mfma_f32_32x32x64_f8f6f4 v[2:17], v[108:115], v[116:123], v[2:17]
	ds_read_b128 v[218:221], v185 offset:16384
	ds_read_b128 v[222:225], v186 offset:16384
	ds_read_b128 v[242:245], v187 offset:16384
	ds_read_b128 v[246:249], v188 offset:16384
	v_mul_f32_e32 v250, s50, v71
	v_fmamk_f32 v251, v250, 0xcb400000, v200
	s_add_i32 m0, s31, 16384
	v_fma_f32 v84, v84, v250, v251
	global_load_lds_dwordx4 v255, s[60:61]
	s_add_i32 m0, s31, 24576
	v_fma_f32 v85, v85, v250, v251
	global_load_lds_dwordx4 v201, s[60:61]
	v_fma_f32 v86, v86, v250, v251
	v_fma_f32 v87, v87, v250, v251
	v_exp_f32_e32 v84, v84
	v_exp_f32_e32 v85, v85
	v_exp_f32_e32 v86, v86
	v_exp_f32_e32 v87, v87
	v_fma_f32 v88, v88, v250, v251
	v_fma_f32 v89, v89, v250, v251
	v_fma_f32 v90, v90, v250, v251
	v_fma_f32 v91, v91, v250, v251
	s_waitcnt lgkmcnt(8)
	v_mfma_f32_32x32x64_f8f6f4 v[18:33], v[108:115], v[124:131], v[18:33]
	v_add_f32_e32 v67, v84, v85
	v_add_f32_e32 v68, v86, v87
	v_exp_f32_e32 v88, v88
	v_exp_f32_e32 v89, v89
	v_exp_f32_e32 v90, v90
	v_exp_f32_e32 v91, v91
	v_add_f32_e32 v67, v67, v68
	v_cvt_pk_fp8_f32 v164, v84, v85
	v_cvt_pk_fp8_f32 v164, v86, v87 op_sel:[0,0,1]
	v_fma_f32 v92, v92, v250, v251
	v_fma_f32 v93, v93, v250, v251
	v_fma_f32 v94, v94, v250, v251
	v_fma_f32 v95, v95, v250, v251
	v_add_f32_e32 v68, v88, v89
	v_add_f32_e32 v69, v90, v91
	s_waitcnt lgkmcnt(6)
	v_mfma_f32_32x32x64_f8f6f4 v[50:65], v[108:115], v[202:209], v[50:65]
	ds_read_b128 v[202:205], v189 offset:16384
	ds_read_b128 v[206:209], v190 offset:16384
	v_exp_f32_e32 v92, v92
	v_exp_f32_e32 v93, v93
	v_exp_f32_e32 v94, v94
	v_exp_f32_e32 v95, v95
	v_add_f32_e32 v68, v68, v69
	v_cvt_pk_fp8_f32 v165, v88, v89
	v_cvt_pk_fp8_f32 v165, v90, v91 op_sel:[0,0,1]
	v_fma_f32 v96, v96, v250, v251
	v_fma_f32 v97, v97, v250, v251
	v_fma_f32 v98, v98, v250, v251
	v_fma_f32 v99, v99, v250, v251
	v_add_f32_e32 v67, v67, v68
	v_add_f32_e32 v68, v92, v93
	v_add_f32_e32 v69, v94, v95
	s_waitcnt lgkmcnt(6)
	v_mfma_f32_32x32x64_f8f6f4 v[34:49], v[108:115], v[210:217], v[34:49]
	ds_read_b128 v[210:213], v191 offset:16384
	ds_read_b128 v[214:217], v192 offset:16384
	v_exp_f32_e32 v96, v96
	v_exp_f32_e32 v97, v97
	v_exp_f32_e32 v98, v98
	v_exp_f32_e32 v99, v99
	v_add_f32_e32 v68, v68, v69
	v_cvt_pk_fp8_f32 v166, v92, v93
	v_cvt_pk_fp8_f32 v166, v94, v95 op_sel:[0,0,1]
	v_add_f32_e32 v67, v67, v68
	v_add_f32_e32 v68, v96, v97
	v_add_f32_e32 v69, v98, v99
	s_add_u32 s60, s60, 0x4000
	s_addc_u32 s61, s61, 0
	v_add_f32_e32 v68, v68, v69
	v_cvt_pk_fp8_f32 v167, v96, v97
	v_cvt_pk_fp8_f32 v167, v98, v99 op_sel:[0,0,1]
	v_add_f32_e32 v67, v67, v68
	ds_write_b128 v194, v[164:167] offset:8192
	v_max_f32_e32 v72, v72, v67
	v_add_f32_e32 v66, v66, v67
	s_add_i32 s43, s43, 1
	s_waitcnt lgkmcnt(7)
	v_mfma_i32_32x32x32_i8 v[84:99], v[218:221], v[132:135], v[226:241]
	v_mfma_i32_32x32x32_i8 v[84:99], v[222:225], v[136:139], v[84:99]
	s_waitcnt vmcnt(2) lgkmcnt(0)
	s_barrier
.Lat_u3:
	ds_read_b128 v[108:111], v193 offset:8192
	ds_read_b128 v[112:115], v193 offset:9216
	v_mfma_i32_32x32x32_i8 v[84:99], v[242:245], v[140:143], v[84:99]
	ds_read_b128 v[116:119], v195 offset:6144
	ds_read_b128 v[120:123], v196 offset:6144
	s_add_i32 m0, s31, 49152
	ds_read_b128 v[124:127], v195 offset:4096
	global_load_lds_dwordx4 v252, s[60:61]
	s_add_i32 m0, s31, 57344
	v_mfma_i32_32x32x32_i8 v[84:99], v[246:249], v[144:147], v[84:99]
	global_load_lds_dwordx4 v254, s[60:61]
	ds_read_b128 v[128:131], v196 offset:4096
	v_mfma_i32_32x32x32_i8 v[84:99], v[202:205], v[148:151], v[84:99]
	ds_read_b128 v[202:205], v195
	v_mfma_i32_32x32x32_i8 v[84:99], v[206:209], v[152:155], v[84:99]
	ds_read_b128 v[206:209], v196
	v_mfma_i32_32x32x32_i8 v[84:99], v[210:213], v[156:159], v[84:99]
	ds_read_b128 v[210:213], v195 offset:2048
	v_mfma_i32_32x32x32_i8 v[84:99], v[214:217], v[160:163], v[84:99]
	ds_read_b128 v[214:217], v196 offset:2048
	v_readlane_b32 s50, v182, s43
	s_waitcnt lgkmcnt(6)
	v_mfma_f32_32x32x64_f8f6f4 v[2:17], v[108:115], v[116:123], v[2:17]
	ds_read_b128 v[218:221], v185 offset:32768
	ds_read_b128 v[222:225], v186 offset:32768
	ds_read_b128 v[242:245], v187 offset:32768
	ds_read_b128 v[246:249], v188 offset:32768
	v_mul_f32_e32 v250, s50, v71
	v_fmamk_f32 v251, v250, 0xcb400000, v200
	s_add_i32 m0, s31, 32768
	v_fma_f32 v84, v84, v250, v251
	global_load_lds_dwordx4 v255, s[60:61]
	s_add_i32 m0, s31, 40960
	v_fma_f32 v85, v85, v250, v251
	global_load_lds_dwordx4 v201, s[60:61]
	v_fma_f32 v86, v86, v250, v251
	v_fma_f32 v87, v87, v250, v251
	v_exp_f32_e32 v84, v84
	v_exp_f32_e32 v85, v85
	v_exp_f32_e32 v86, v86
	v_exp_f32_e32 v87, v87
	v_fma_f32 v88, v88, v250, v251
	v_fma_f32 v89, v89, v250, v251
	v_fma_f32 v90, v90, v250, v251
	v_fma_f32 v91, v91, v250, v251
	s_waitcnt lgkmcnt(8)
	v_mfma_f32_32x32x64_f8f6f4 v[18:33], v[108:115], v[124:131], v[18:33]
	v_add_f32_e32 v67, v84, v85
	v_add_f32_e32 v68, v86, v87
	v_exp_f32_e32 v88, v88
	v_exp_f32_e32 v89, v89
	v_exp_f32_e32 v90, v90
	v_exp_f32_e32 v91, v91
	v_add_f32_e32 v67, v67, v68
	v_cvt_pk_fp8_f32 v164, v84, v85
	v_cvt_pk_fp8_f32 v164, v86, v87 op_sel:[0,0,1]
	v_fma_f32 v92, v92, v250, v251
	v_fma_f32 v93, v93, v250, v251
	v_fma_f32 v94, v94, v250, v251
	v_fma_f32 v95, v95, v250, v251
	v_add_f32_e32 v68, v88, v89
	v_add_f32_e32 v69, v90, v91
	s_waitcnt lgkmcnt(6)
	v_mfma_f32_32x32x64_f8f6f4 v[50:65], v[108:115], v[202:209], v[50:65]
	ds_read_b128 v[202:205], v189 offset:32768
	ds_read_b128 v[206:209], v190 offset:32768
	v_exp_f32_e32 v92, v92
	v_exp_f32_e32 v93, v93
	v_exp_f32_e32 v94, v94
	v_exp_f32_e32 v95, v95
	v_add_f32_e32 v68, v68, v69
	v_cvt_pk_fp8_f32 v165, v88, v89
	v_cvt_pk_fp8_f32 v165, v90, v91 op_sel:[0,0,1]
	v_fma_f32 v96, v96, v250, v251
	v_fma_f32 v97, v97, v250, v251
	v_fma_f32 v98, v98, v250, v251
	v_fma_f32 v99, v99, v250, v251
	v_add_f32_e32 v67, v67, v68
	v_add_f32_e32 v68, v92, v93
	v_add_f32_e32 v69, v94, v95
	s_waitcnt lgkmcnt(6)
	v_mfma_f32_32x32x64_f8f6f4 v[34:49], v[108:115], v[210:217], v[34:49]
	ds_read_b128 v[210:213], v191 offset:32768
	ds_read_b128 v[214:217], v192 offset:32768
	v_exp_f32_e32 v96, v96
	v_exp_f32_e32 v97, v97
	v_exp_f32_e32 v98, v98
	v_exp_f32_e32 v99, v99
	v_add_f32_e32 v68, v68, v69
	v_cvt_pk_fp8_f32 v166, v92, v93
	v_cvt_pk_fp8_f32 v166, v94, v95 op_sel:[0,0,1]
	v_add_f32_e32 v67, v67, v68
	v_add_f32_e32 v68, v96, v97
	v_add_f32_e32 v69, v98, v99
	s_add_u32 s60, s60, 0x4000
	s_addc_u32 s61, s61, 0
	v_add_f32_e32 v68, v68, v69
	v_cvt_pk_fp8_f32 v167, v96, v97
	v_cvt_pk_fp8_f32 v167, v98, v99 op_sel:[0,0,1]
	v_add_f32_e32 v67, v67, v68
	ds_write_b128 v194, v[164:167]
	v_max_f32_e32 v72, v72, v67
	v_add_f32_e32 v66, v66, v67
	s_add_i32 s43, s43, 1
	s_waitcnt lgkmcnt(7)
	v_mfma_i32_32x32x32_i8 v[84:99], v[218:221], v[132:135], v[226:241]
	v_mfma_i32_32x32x32_i8 v[84:99], v[222:225], v[136:139], v[84:99]
	s_waitcnt vmcnt(2) lgkmcnt(0)
	s_barrier
.Lat_u4:
	ds_read_b128 v[108:111], v193
	ds_read_b128 v[112:115], v193 offset:1024
	v_mfma_i32_32x32x32_i8 v[84:99], v[242:245], v[140:143], v[84:99]
	ds_read_b128 v[116:119], v195 offset:22528
	ds_read_b128 v[120:123], v196 offset:22528
	s_add_i32 m0, s31, 65536
	ds_read_b128 v[124:127], v195 offset:20480
	global_load_lds_dwordx4 v252, s[60:61]
	s_add_i32 m0, s31, 73728
	v_mfma_i32_32x32x32_i8 v[84:99], v[246:249], v[144:147], v[84:99]
	global_load_lds_dwordx4 v254, s[60:61]
	ds_read_b128 v[128:131], v196 offset:20480
	v_mfma_i32_32x32x32_i8 v[84:99], v[202:205], v[148:151], v[84:99]
	ds_read_b128 v[202:205], v195 offset:16384
	v_mfma_i32_32x32x32_i8 v[84:99], v[206:209], v[152:155], v[84:99]
	ds_read_b128 v[206:209], v196 offset:16384
	v_mfma_i32_32x32x32_i8 v[84:99], v[210:213], v[156:159], v[84:99]
	ds_read_b128 v[210:213], v195 offset:18432
	v_mfma_i32_32x32x32_i8 v[84:99], v[214:217], v[160:163], v[84:99]
	ds_read_b128 v[214:217], v196 offset:18432
	v_readlane_b32 s50, v182, s43
	s_waitcnt lgkmcnt(6)
	v_mfma_f32_32x32x64_f8f6f4 v[2:17], v[108:115], v[116:123], v[2:17]
	ds_read_b128 v[218:221], v185
	ds_read_b128 v[222:225], v186
	ds_read_b128 v[242:245], v187
	ds_read_b128 v[246:249], v188
	v_mul_f32_e32 v250, s50, v71
	v_fmamk_f32 v251, v250, 0xcb400000, v200
	s_mov_b32 m0, s31
	v_fma_f32 v84, v84, v250, v251
	global_load_lds_dwordx4 v255, s[60:61]
	s_add_i32 m0, s31, 8192
	v_fma_f32 v85, v85, v250, v251
	global_load_lds_dwordx4 v201, s[60:61]
	v_fma_f32 v86, v86, v250, v251
	v_fma_f32 v87, v87, v250, v251
	v_exp_f32_e32 v84, v84
	v_exp_f32_e32 v85, v85
	v_exp_f32_e32 v86, v86
	v_exp_f32_e32 v87, v87
	v_fma_f32 v88, v88, v250, v251
	v_fma_f32 v89, v89, v250, v251
	v_fma_f32 v90, v90, v250, v251
	v_fma_f32 v91, v91, v250, v251
	s_waitcnt lgkmcnt(8)
	v_mfma_f32_32x32x64_f8f6f4 v[18:33], v[108:115], v[124:131], v[18:33]
	v_add_f32_e32 v67, v84, v85
	v_add_f32_e32 v68, v86, v87
	v_exp_f32_e32 v88, v88
	v_exp_f32_e32 v89, v89
	v_exp_f32_e32 v90, v90
	v_exp_f32_e32 v91, v91
	v_add_f32_e32 v67, v67, v68
	v_cvt_pk_fp8_f32 v164, v84, v85
	v_cvt_pk_fp8_f32 v164, v86, v87 op_sel:[0,0,1]
	v_fma_f32 v92, v92, v250, v251
	v_fma_f32 v93, v93, v250, v251
	v_fma_f32 v94, v94, v250, v251
	v_fma_f32 v95, v95, v250, v251
	v_add_f32_e32 v68, v88, v89
	v_add_f32_e32 v69, v90, v91
	s_waitcnt lgkmcnt(6)
	v_mfma_f32_32x32x64_f8f6f4 v[50:65], v[108:115], v[202:209], v[50:65]
	ds_read_b128 v[202:205], v189
	ds_read_b128 v[206:209], v190
	v_exp_f32_e32 v92, v92
	v_exp_f32_e32 v93, v93
	v_exp_f32_e32 v94, v94
	v_exp_f32_e32 v95, v95
	v_add_f32_e32 v68, v68, v69
	v_cvt_pk_fp8_f32 v165, v88, v89
	v_cvt_pk_fp8_f32 v165, v90, v91 op_sel:[0,0,1]
	v_fma_f32 v96, v96, v250, v251
	v_fma_f32 v97, v97, v250, v251
	v_fma_f32 v98, v98, v250, v251
	v_fma_f32 v99, v99, v250, v251
	v_add_f32_e32 v67, v67, v68
	v_add_f32_e32 v68, v92, v93
	v_add_f32_e32 v69, v94, v95
	s_waitcnt lgkmcnt(6)
	v_mfma_f32_32x32x64_f8f6f4 v[34:49], v[108:115], v[210:217], v[34:49]
	ds_read_b128 v[210:213], v191
	ds_read_b128 v[214:217], v192
	v_exp_f32_e32 v96, v96
	v_exp_f32_e32 v97, v97
	v_exp_f32_e32 v98, v98
	v_exp_f32_e32 v99, v99
	v_add_f32_e32 v68, v68, v69
	v_cvt_pk_fp8_f32 v166, v92, v93
	v_cvt_pk_fp8_f32 v166, v94, v95 op_sel:[0,0,1]
	v_add_f32_e32 v67, v67, v68
	v_add_f32_e32 v68, v96, v97
	v_add_f32_e32 v69, v98, v99
	s_add_u32 s60, s60, 0x4000
	s_addc_u32 s61, s61, 0
	v_add_f32_e32 v68, v68, v69
	v_cvt_pk_fp8_f32 v167, v96, v97
	v_cvt_pk_fp8_f32 v167, v98, v99 op_sel:[0,0,1]
	v_add_f32_e32 v67, v67, v68
	ds_write_b128 v194, v[164:167] offset:8192
	v_max_f32_e32 v72, v72, v67
	v_add_f32_e32 v66, v66, v67
	s_add_i32 s43, s43, 1
	s_waitcnt lgkmcnt(7)
	v_mfma_i32_32x32x32_i8 v[84:99], v[218:221], v[132:135], v[226:241]
	v_mfma_i32_32x32x32_i8 v[84:99], v[222:225], v[136:139], v[84:99]
	s_waitcnt vmcnt(2) lgkmcnt(0)
	s_barrier

.Lat_k5:
	ds_read_b128 v[128:131], v196 offset:36864
	v_mfma_i32_32x32x32_i8 v[84:99], v[202:205], v[148:151], v[84:99]
	ds_read_b128 v[202:205], v195 offset:32768
	v_mfma_i32_32x32x32_i8 v[84:99], v[206:209], v[152:155], v[84:99]
	ds_read_b128 v[206:209], v196 offset:32768
	v_mfma_i32_32x32x32_i8 v[84:99], v[210:213], v[156:159], v[84:99]
	ds_read_b128 v[210:213], v195 offset:34816
	v_mfma_i32_32x32x32_i8 v[84:99], v[214:217], v[160:163], v[84:99]
	ds_read_b128 v[214:217], v196 offset:34816
	v_readlane_b32 s50, v182, s43
	s_waitcnt lgkmcnt(6)
	v_mfma_f32_32x32x64_f8f6f4 v[2:17], v[108:115], v[116:123], v[2:17]
	ds_read_b128 v[218:221], v185 offset:16384
	ds_read_b128 v[222:225], v186 offset:16384
	ds_read_b128 v[242:245], v187 offset:16384
	ds_read_b128 v[246:249], v188 offset:16384
	v_mul_f32_e32 v250, s50, v71
	v_fmamk_f32 v251, v250, 0xcb400000, v200
	s_add_i32 m0, s31, 16384
	v_fma_f32 v84, v84, v250, v251
	global_load_lds_dwordx4 v255, s[60:61]
	s_add_i32 m0, s31, 24576
	v_fma_f32 v85, v85, v250, v251
	global_load_lds_dwordx4 v201, s[60:61]
	v_fma_f32 v86, v86, v250, v251
	v_fma_f32 v87, v87, v250, v251
	v_exp_f32_e32 v84, v84
	v_exp_f32_e32 v85, v85
	v_exp_f32_e32 v86, v86
	v_exp_f32_e32 v87, v87
	v_fma_f32 v88, v88, v250, v251
	v_fma_f32 v89, v89, v250, v251
	v_fma_f32 v90, v90, v250, v251
	v_fma_f32 v91, v91, v250, v251
	s_waitcnt lgkmcnt(8)
	v_mfma_f32_32x32x64_f8f6f4 v[18:33], v[108:115], v[124:131], v[18:33]
	v_add_f32_e32 v67, v84, v85
	v_add_f32_e32 v68, v86, v87
	v_exp_f32_e32 v88, v88
	v_exp_f32_e32 v89, v89
	v_exp_f32_e32 v90, v90
	v_exp_f32_e32 v91, v91
	v_add_f32_e32 v67, v67, v68
	v_cvt_pk_fp8_f32 v164, v84, v85
	v_cvt_pk_fp8_f32 v164, v86, v87 op_sel:[0,0,1]
	v_fma_f32 v92, v92, v250, v251
	v_fma_f32 v93, v93, v250, v251
	v_fma_f32 v94, v94, v250, v251
	v_fma_f32 v95, v95, v250, v251
	v_add_f32_e32 v68, v88, v89
	v_add_f32_e32 v69, v90, v91
	s_waitcnt lgkmcnt(6)
	v_mfma_f32_32x32x64_f8f6f4 v[50:65], v[108:115], v[202:209], v[50:65]
	ds_read_b128 v[202:205], v189 offset:16384
	ds_read_b128 v[206:209], v190 offset:16384
	v_exp_f32_e32 v92, v92
	v_exp_f32_e32 v93, v93
	v_exp_f32_e32 v94, v94
	v_exp_f32_e32 v95, v95
	v_add_f32_e32 v68, v68, v69
	v_cvt_pk_fp8_f32 v165, v88, v89
	v_cvt_pk_fp8_f32 v165, v90, v91 op_sel:[0,0,1]
	v_fma_f32 v96, v96, v250, v251
	v_fma_f32 v97, v97, v250, v251
	v_fma_f32 v98, v98, v250, v251
	v_fma_f32 v99, v99, v250, v251
	v_add_f32_e32 v67, v67, v68
	v_add_f32_e32 v68, v92, v93
	v_add_f32_e32 v69, v94, v95
	s_waitcnt lgkmcnt(6)
	v_mfma_f32_32x32x64_f8f6f4 v[34:49], v[108:115], v[210:217], v[34:49]
	ds_read_b128 v[210:213], v191 offset:16384
	ds_read_b128 v[214:217], v192 offset:16384
	v_exp_f32_e32 v96, v96
	v_exp_f32_e32 v97, v97
	v_exp_f32_e32 v98, v98
	v_exp_f32_e32 v99, v99
	v_add_f32_e32 v68, v68, v69
	v_cvt_pk_fp8_f32 v166, v92, v93
	v_cvt_pk_fp8_f32 v166, v94, v95 op_sel:[0,0,1]
	v_add_f32_e32 v67, v67, v68
	v_add_f32_e32 v68, v96, v97
	v_add_f32_e32 v69, v98, v99
	s_add_u32 s60, s60, 0x4000
	s_addc_u32 s61, s61, 0
	v_add_f32_e32 v68, v68, v69
	v_cvt_pk_fp8_f32 v167, v96, v97
	v_cvt_pk_fp8_f32 v167, v98, v99 op_sel:[0,0,1]
	v_add_f32_e32 v67, v67, v68
	ds_write_b128 v194, v[164:167]
	v_max_f32_e32 v72, v72, v67
	v_add_f32_e32 v66, v66, v67
	s_add_i32 s43, s43, 1
	s_waitcnt lgkmcnt(7)
	v_mfma_i32_32x32x32_i8 v[84:99], v[218:221], v[132:135], v[226:241]
	v_mfma_i32_32x32x32_i8 v[84:99], v[222:225], v[136:139], v[84:99]
	s_cmp_gt_u32 s43, 30
	s_cbranch_scc1 .Lat_drain
	s_waitcnt vmcnt(2) lgkmcnt(0)
	s_barrier
	s_branch .Lat_u0

.Lat_last:
	s_waitcnt vmcnt(0) lgkmcnt(0)
	s_barrier
	v_cmp_ge_f32_e64 s[54:55], s42, v72
	s_nop 3
	s_cmp_lg_u64 s[54:55], exec
	s_cselect_b32 s1, 1, 0
	s_or_b32 s39, s39, s1
	v_add_u32_e32 v250, 0xc000, v184
	v_sub_u32_e32 v185, v185, v250
	v_sub_u32_e32 v186, v186, v250
	v_sub_u32_e32 v187, v187, v250
	v_sub_u32_e32 v188, v188, v250
	v_sub_u32_e32 v189, v189, v250
	v_sub_u32_e32 v190, v190, v250
	v_sub_u32_e32 v191, v191, v250
	v_sub_u32_e32 v192, v192, v250
